# v37c
# baseline (speedup 1.0000x reference)
.LBB0_31:
	s_or_b64 exec, exec, s[4:5]
	s_movk_i32 s3, 0xc4
	v_cmp_gt_u32_e32 vcc, s3, v0
	s_waitcnt lgkmcnt(0)
	s_barrier
	s_and_saveexec_b64 s[4:5], vcc
	s_cbranch_execz .LBB0_34
	s_load_dwordx2 s[0:1], s[0:1], 0x28
	ds_read_b32 v2, v2
	v_lshl_add_u32 v0, v0, 8, s2
	v_ashrrev_i32_e32 v1, 31, v0
	s_waitcnt lgkmcnt(0)
	v_lshl_add_u64 v[0:1], v[0:1], 1, s[0:1]
	global_store_short v[0:1], v2, off
	s_endpgm

.LBB1_13:
	s_or_b64 exec, exec, s[10:11]
	v_and_b32_e32 v109, 63, v0
	v_lshrrev_b32_e32 v111, 6, v0
	v_lshlrev_b32_e32 v110, 2, v109
	v_lshlrev_b32_e32 v2, 3, v109
	v_lshl_add_u32 v2, v111, 9, v2
	s_waitcnt lgkmcnt(0)
	global_load_dwordx2 v[10:11], v2, s[4:5]
	v_add_u32_e32 v3, 0x1000, v2
	global_load_dwordx2 v[12:13], v3, s[4:5]
	v_add_u32_e32 v3, 0x2000, v2
	global_load_dwordx2 v[14:15], v3, s[4:5]
	v_add_u32_e32 v3, 0x3000, v2
	global_load_dwordx2 v[16:17], v3, s[4:5]
	v_add_u32_e32 v3, 0x4000, v2
	global_load_dwordx2 v[18:19], v3, s[4:5]
	v_add_u32_e32 v3, 0x5000, v2
	global_load_dwordx2 v[20:21], v3, s[4:5]
	v_add_u32_e32 v3, 0x6000, v2
	global_load_dwordx2 v[22:23], v3, s[4:5]
	v_add_u32_e32 v3, 0x7000, v2
	global_load_dwordx2 v[24:25], v3, s[4:5]
	v_add_u32_e32 v3, 0x8000, v2
	global_load_dwordx2 v[26:27], v3, s[4:5]
	v_add_u32_e32 v3, 0x9000, v2
	global_load_dwordx2 v[28:29], v3, s[4:5]
	v_add_u32_e32 v3, 0xa000, v2
	global_load_dwordx2 v[30:31], v3, s[4:5]
	v_add_u32_e32 v3, 0xb000, v2
	global_load_dwordx2 v[32:33], v3, s[4:5]
	v_add_u32_e32 v3, 0xc000, v2
	global_load_dwordx2 v[34:35], v3, s[4:5]
	v_add_u32_e32 v3, 0xd000, v2
	global_load_dwordx2 v[36:37], v3, s[4:5]
	v_add_u32_e32 v3, 0xe000, v2
	global_load_dwordx2 v[38:39], v3, s[4:5]
	v_add_u32_e32 v3, 0xf000, v2
	global_load_dwordx2 v[40:41], v3, s[4:5]
	v_add_u32_e32 v3, 0x10000, v2
	global_load_dwordx2 v[42:43], v3, s[4:5]
	v_add_u32_e32 v3, 0x11000, v2
	global_load_dwordx2 v[44:45], v3, s[4:5]
	v_add_u32_e32 v3, 0x12000, v2
	global_load_dwordx2 v[46:47], v3, s[4:5]
	v_add_u32_e32 v3, 0x13000, v2
	global_load_dwordx2 v[48:49], v3, s[4:5]
	v_add_u32_e32 v3, 0x14000, v2
	global_load_dwordx2 v[50:51], v3, s[4:5]
	v_add_u32_e32 v3, 0x15000, v2
	global_load_dwordx2 v[52:53], v3, s[4:5]
	v_add_u32_e32 v3, 0x16000, v2
	global_load_dwordx2 v[54:55], v3, s[4:5]
	v_add_u32_e32 v3, 0x17000, v2
	global_load_dwordx2 v[56:57], v3, s[4:5]
	v_add_u32_e32 v3, 0x18000, v2
	global_load_dwordx2 v[58:59], v3, s[4:5]
	v_sub_u32_e32 v6, s31, v110
	v_mov_b32_e32 v7, 0xffff
	v_mov_b32_e32 v8, 0xffff0000
	v_cmp_lt_i32_e64 s[6:7], 0, v6
	v_cmp_lt_i32_e64 s[8:9], 1, v6
	v_cmp_lt_i32_e64 s[10:11], 2, v6
	v_cmp_lt_i32_e64 s[12:13], 3, v6
	v_cndmask_b32_e64 v4, 0, v7, s[6:7]
	v_cndmask_b32_e64 v9, 0, v8, s[8:9]
	v_cndmask_b32_e64 v5, 0, v7, s[10:11]
	v_cndmask_b32_e64 v6, 0, v8, s[12:13]
	v_or_b32_e32 v4, v4, v9
	v_or_b32_e32 v5, v5, v6
	v_and_b32_e32 v9, 15, v0
	v_cmp_eq_u32_e64 s[16:17], 0, v9
	v_lshrrev_b32_e32 v9, 1, v109
	v_lshl_or_b32 v98, v111, 5, v9
	v_readfirstlane_b32 s14, v111
	s_cmp_lt_u32 s14, 4
	s_cselect_b64 s[18:19], s[16:17], 0
	s_waitcnt vmcnt(24)
	v_add_u32_e32 v60, v10, v11
	v_and_b32_e32 v61, v4, v10
	v_and_b32_e32 v62, v5, v11
	v_add_u32_e32 v61, v61, v62
	v_add_u32_sdwa v62, v60, v60 dst_sel:DWORD dst_unused:UNUSED_PAD src0_sel:WORD_0 src1_sel:WORD_1
	v_add_u32_sdwa v63, v61, v61 dst_sel:DWORD dst_unused:UNUSED_PAD src0_sel:WORD_0 src1_sel:WORD_1
	s_nop 0
	v_add_u32_dpp v62, v62, v62 quad_perm:[1,0,3,2] row_mask:0xf bank_mask:0xf bound_ctrl:1
	v_add_u32_dpp v63, v63, v63 quad_perm:[1,0,3,2] row_mask:0xf bank_mask:0xf bound_ctrl:1
	s_nop 0
	v_add_u32_dpp v62, v62, v62 quad_perm:[2,3,0,1] row_mask:0xf bank_mask:0xf bound_ctrl:1
	v_add_u32_dpp v63, v63, v63 quad_perm:[2,3,0,1] row_mask:0xf bank_mask:0xf bound_ctrl:1
	s_nop 0
	v_add_u32_dpp v62, v62, v62 row_half_mirror row_mask:0xf bank_mask:0xf bound_ctrl:1
	v_add_u32_dpp v63, v63, v63 row_half_mirror row_mask:0xf bank_mask:0xf bound_ctrl:1
	s_nop 0
	v_mov_b32_dpp v64, v62 row_mirror row_mask:0xf bank_mask:0xf bound_ctrl:1
	v_mov_b32_dpp v65, v63 row_mirror row_mask:0xf bank_mask:0xf bound_ctrl:1
	s_mov_b64 exec, s[16:17]
	v_add_u32_e32 v64, v64, v62
	v_add_u32_e32 v65, v65, v63
	ds_write_b64 v98, v[64:65]
	s_mov_b64 exec, -1
	s_waitcnt vmcnt(23)
	v_add_u32_e32 v60, v12, v13
	v_and_b32_e32 v61, v4, v12
	v_and_b32_e32 v62, v5, v13
	v_add_u32_e32 v61, v61, v62
	v_add_u32_sdwa v62, v60, v60 dst_sel:DWORD dst_unused:UNUSED_PAD src0_sel:WORD_0 src1_sel:WORD_1
	v_add_u32_sdwa v63, v61, v61 dst_sel:DWORD dst_unused:UNUSED_PAD src0_sel:WORD_0 src1_sel:WORD_1
	s_nop 0
	v_add_u32_dpp v62, v62, v62 quad_perm:[1,0,3,2] row_mask:0xf bank_mask:0xf bound_ctrl:1
	v_add_u32_dpp v63, v63, v63 quad_perm:[1,0,3,2] row_mask:0xf bank_mask:0xf bound_ctrl:1
	s_nop 0
	v_add_u32_dpp v62, v62, v62 quad_perm:[2,3,0,1] row_mask:0xf bank_mask:0xf bound_ctrl:1
	v_add_u32_dpp v63, v63, v63 quad_perm:[2,3,0,1] row_mask:0xf bank_mask:0xf bound_ctrl:1
	s_nop 0
	v_add_u32_dpp v62, v62, v62 row_half_mirror row_mask:0xf bank_mask:0xf bound_ctrl:1
	v_add_u32_dpp v63, v63, v63 row_half_mirror row_mask:0xf bank_mask:0xf bound_ctrl:1
	s_nop 0
	v_mov_b32_dpp v64, v62 row_mirror row_mask:0xf bank_mask:0xf bound_ctrl:1
	v_mov_b32_dpp v65, v63 row_mirror row_mask:0xf bank_mask:0xf bound_ctrl:1
	s_mov_b64 exec, s[16:17]
	v_add_u32_e32 v64, v64, v62
	v_add_u32_e32 v65, v65, v63
	ds_write_b64 v98, v[64:65] offset:256
	s_mov_b64 exec, -1
	s_waitcnt vmcnt(22)
	v_add_u32_e32 v60, v14, v15
	v_and_b32_e32 v61, v4, v14
	v_and_b32_e32 v62, v5, v15
	v_add_u32_e32 v61, v61, v62
	v_add_u32_sdwa v62, v60, v60 dst_sel:DWORD dst_unused:UNUSED_PAD src0_sel:WORD_0 src1_sel:WORD_1
	v_add_u32_sdwa v63, v61, v61 dst_sel:DWORD dst_unused:UNUSED_PAD src0_sel:WORD_0 src1_sel:WORD_1
	s_nop 0
	v_add_u32_dpp v62, v62, v62 quad_perm:[1,0,3,2] row_mask:0xf bank_mask:0xf bound_ctrl:1
	v_add_u32_dpp v63, v63, v63 quad_perm:[1,0,3,2] row_mask:0xf bank_mask:0xf bound_ctrl:1
	s_nop 0
	v_add_u32_dpp v62, v62, v62 quad_perm:[2,3,0,1] row_mask:0xf bank_mask:0xf bound_ctrl:1
	v_add_u32_dpp v63, v63, v63 quad_perm:[2,3,0,1] row_mask:0xf bank_mask:0xf bound_ctrl:1
	s_nop 0
	v_add_u32_dpp v62, v62, v62 row_half_mirror row_mask:0xf bank_mask:0xf bound_ctrl:1
	v_add_u32_dpp v63, v63, v63 row_half_mirror row_mask:0xf bank_mask:0xf bound_ctrl:1
	s_nop 0
	v_mov_b32_dpp v64, v62 row_mirror row_mask:0xf bank_mask:0xf bound_ctrl:1
	v_mov_b32_dpp v65, v63 row_mirror row_mask:0xf bank_mask:0xf bound_ctrl:1
	s_mov_b64 exec, s[16:17]
	v_add_u32_e32 v64, v64, v62
	v_add_u32_e32 v65, v65, v63
	ds_write_b64 v98, v[64:65] offset:512
	s_mov_b64 exec, -1
	s_waitcnt vmcnt(21)
	v_add_u32_e32 v60, v16, v17
	v_and_b32_e32 v61, v4, v16
	v_and_b32_e32 v62, v5, v17
	v_add_u32_e32 v61, v61, v62
	v_add_u32_sdwa v62, v60, v60 dst_sel:DWORD dst_unused:UNUSED_PAD src0_sel:WORD_0 src1_sel:WORD_1
	v_add_u32_sdwa v63, v61, v61 dst_sel:DWORD dst_unused:UNUSED_PAD src0_sel:WORD_0 src1_sel:WORD_1
	s_nop 0
	v_add_u32_dpp v62, v62, v62 quad_perm:[1,0,3,2] row_mask:0xf bank_mask:0xf bound_ctrl:1
	v_add_u32_dpp v63, v63, v63 quad_perm:[1,0,3,2] row_mask:0xf bank_mask:0xf bound_ctrl:1
	s_nop 0
	v_add_u32_dpp v62, v62, v62 quad_perm:[2,3,0,1] row_mask:0xf bank_mask:0xf bound_ctrl:1
	v_add_u32_dpp v63, v63, v63 quad_perm:[2,3,0,1] row_mask:0xf bank_mask:0xf bound_ctrl:1
	s_nop 0
	v_add_u32_dpp v62, v62, v62 row_half_mirror row_mask:0xf bank_mask:0xf bound_ctrl:1
	v_add_u32_dpp v63, v63, v63 row_half_mirror row_mask:0xf bank_mask:0xf bound_ctrl:1
	s_nop 0
	v_mov_b32_dpp v64, v62 row_mirror row_mask:0xf bank_mask:0xf bound_ctrl:1
	v_mov_b32_dpp v65, v63 row_mirror row_mask:0xf bank_mask:0xf bound_ctrl:1
	s_mov_b64 exec, s[16:17]
	v_add_u32_e32 v64, v64, v62
	v_add_u32_e32 v65, v65, v63
	ds_write_b64 v98, v[64:65] offset:768
	s_mov_b64 exec, -1
	s_waitcnt vmcnt(20)
	v_add_u32_e32 v60, v18, v19
	v_and_b32_e32 v61, v4, v18
	v_and_b32_e32 v62, v5, v19
	v_add_u32_e32 v61, v61, v62
	v_add_u32_sdwa v62, v60, v60 dst_sel:DWORD dst_unused:UNUSED_PAD src0_sel:WORD_0 src1_sel:WORD_1
	v_add_u32_sdwa v63, v61, v61 dst_sel:DWORD dst_unused:UNUSED_PAD src0_sel:WORD_0 src1_sel:WORD_1
	s_nop 0
	v_add_u32_dpp v62, v62, v62 quad_perm:[1,0,3,2] row_mask:0xf bank_mask:0xf bound_ctrl:1
	v_add_u32_dpp v63, v63, v63 quad_perm:[1,0,3,2] row_mask:0xf bank_mask:0xf bound_ctrl:1
	s_nop 0
	v_add_u32_dpp v62, v62, v62 quad_perm:[2,3,0,1] row_mask:0xf bank_mask:0xf bound_ctrl:1
	v_add_u32_dpp v63, v63, v63 quad_perm:[2,3,0,1] row_mask:0xf bank_mask:0xf bound_ctrl:1
	s_nop 0
	v_add_u32_dpp v62, v62, v62 row_half_mirror row_mask:0xf bank_mask:0xf bound_ctrl:1
	v_add_u32_dpp v63, v63, v63 row_half_mirror row_mask:0xf bank_mask:0xf bound_ctrl:1
	s_nop 0
	v_mov_b32_dpp v64, v62 row_mirror row_mask:0xf bank_mask:0xf bound_ctrl:1
	v_mov_b32_dpp v65, v63 row_mirror row_mask:0xf bank_mask:0xf bound_ctrl:1
	s_mov_b64 exec, s[16:17]
	v_add_u32_e32 v64, v64, v62
	v_add_u32_e32 v65, v65, v63
	ds_write_b64 v98, v[64:65] offset:1024
	s_mov_b64 exec, -1
	s_waitcnt vmcnt(19)
	v_add_u32_e32 v60, v20, v21
	v_and_b32_e32 v61, v4, v20
	v_and_b32_e32 v62, v5, v21
	v_add_u32_e32 v61, v61, v62
	v_add_u32_sdwa v62, v60, v60 dst_sel:DWORD dst_unused:UNUSED_PAD src0_sel:WORD_0 src1_sel:WORD_1
	v_add_u32_sdwa v63, v61, v61 dst_sel:DWORD dst_unused:UNUSED_PAD src0_sel:WORD_0 src1_sel:WORD_1
	s_nop 0
	v_add_u32_dpp v62, v62, v62 quad_perm:[1,0,3,2] row_mask:0xf bank_mask:0xf bound_ctrl:1
	v_add_u32_dpp v63, v63, v63 quad_perm:[1,0,3,2] row_mask:0xf bank_mask:0xf bound_ctrl:1
	s_nop 0
	v_add_u32_dpp v62, v62, v62 quad_perm:[2,3,0,1] row_mask:0xf bank_mask:0xf bound_ctrl:1
	v_add_u32_dpp v63, v63, v63 quad_perm:[2,3,0,1] row_mask:0xf bank_mask:0xf bound_ctrl:1
	s_nop 0
	v_add_u32_dpp v62, v62, v62 row_half_mirror row_mask:0xf bank_mask:0xf bound_ctrl:1
	v_add_u32_dpp v63, v63, v63 row_half_mirror row_mask:0xf bank_mask:0xf bound_ctrl:1
	s_nop 0
	v_mov_b32_dpp v64, v62 row_mirror row_mask:0xf bank_mask:0xf bound_ctrl:1
	v_mov_b32_dpp v65, v63 row_mirror row_mask:0xf bank_mask:0xf bound_ctrl:1
	s_mov_b64 exec, s[16:17]
	v_add_u32_e32 v64, v64, v62
	v_add_u32_e32 v65, v65, v63
	ds_write_b64 v98, v[64:65] offset:1280
	s_mov_b64 exec, -1
	s_waitcnt vmcnt(18)
	v_add_u32_e32 v60, v22, v23
	v_and_b32_e32 v61, v4, v22
	v_and_b32_e32 v62, v5, v23
	v_add_u32_e32 v61, v61, v62
	v_add_u32_sdwa v62, v60, v60 dst_sel:DWORD dst_unused:UNUSED_PAD src0_sel:WORD_0 src1_sel:WORD_1
	v_add_u32_sdwa v63, v61, v61 dst_sel:DWORD dst_unused:UNUSED_PAD src0_sel:WORD_0 src1_sel:WORD_1
	s_nop 0
	v_add_u32_dpp v62, v62, v62 quad_perm:[1,0,3,2] row_mask:0xf bank_mask:0xf bound_ctrl:1
	v_add_u32_dpp v63, v63, v63 quad_perm:[1,0,3,2] row_mask:0xf bank_mask:0xf bound_ctrl:1
	s_nop 0
	v_add_u32_dpp v62, v62, v62 quad_perm:[2,3,0,1] row_mask:0xf bank_mask:0xf bound_ctrl:1
	v_add_u32_dpp v63, v63, v63 quad_perm:[2,3,0,1] row_mask:0xf bank_mask:0xf bound_ctrl:1
	s_nop 0
	v_add_u32_dpp v62, v62, v62 row_half_mirror row_mask:0xf bank_mask:0xf bound_ctrl:1
	v_add_u32_dpp v63, v63, v63 row_half_mirror row_mask:0xf bank_mask:0xf bound_ctrl:1
	s_nop 0
	v_mov_b32_dpp v64, v62 row_mirror row_mask:0xf bank_mask:0xf bound_ctrl:1
	v_mov_b32_dpp v65, v63 row_mirror row_mask:0xf bank_mask:0xf bound_ctrl:1
	s_mov_b64 exec, s[16:17]
	v_add_u32_e32 v64, v64, v62
	v_add_u32_e32 v65, v65, v63
	ds_write_b64 v98, v[64:65] offset:1536
	s_mov_b64 exec, -1
	s_waitcnt vmcnt(17)
	v_add_u32_e32 v60, v24, v25
	v_and_b32_e32 v61, v4, v24
	v_and_b32_e32 v62, v5, v25
	v_add_u32_e32 v61, v61, v62
	v_add_u32_sdwa v62, v60, v60 dst_sel:DWORD dst_unused:UNUSED_PAD src0_sel:WORD_0 src1_sel:WORD_1
	v_add_u32_sdwa v63, v61, v61 dst_sel:DWORD dst_unused:UNUSED_PAD src0_sel:WORD_0 src1_sel:WORD_1
	s_nop 0
	v_add_u32_dpp v62, v62, v62 quad_perm:[1,0,3,2] row_mask:0xf bank_mask:0xf bound_ctrl:1
	v_add_u32_dpp v63, v63, v63 quad_perm:[1,0,3,2] row_mask:0xf bank_mask:0xf bound_ctrl:1
	s_nop 0
	v_add_u32_dpp v62, v62, v62 quad_perm:[2,3,0,1] row_mask:0xf bank_mask:0xf bound_ctrl:1
	v_add_u32_dpp v63, v63, v63 quad_perm:[2,3,0,1] row_mask:0xf bank_mask:0xf bound_ctrl:1
	s_nop 0
	v_add_u32_dpp v62, v62, v62 row_half_mirror row_mask:0xf bank_mask:0xf bound_ctrl:1
	v_add_u32_dpp v63, v63, v63 row_half_mirror row_mask:0xf bank_mask:0xf bound_ctrl:1
	s_nop 0
	v_mov_b32_dpp v64, v62 row_mirror row_mask:0xf bank_mask:0xf bound_ctrl:1
	v_mov_b32_dpp v65, v63 row_mirror row_mask:0xf bank_mask:0xf bound_ctrl:1
	s_mov_b64 exec, s[16:17]
	v_add_u32_e32 v64, v64, v62
	v_add_u32_e32 v65, v65, v63
	ds_write_b64 v98, v[64:65] offset:1792
	s_mov_b64 exec, -1
	s_waitcnt vmcnt(16)
	v_add_u32_e32 v60, v26, v27
	v_and_b32_e32 v61, v4, v26
	v_and_b32_e32 v62, v5, v27
	v_add_u32_e32 v61, v61, v62
	v_add_u32_sdwa v62, v60, v60 dst_sel:DWORD dst_unused:UNUSED_PAD src0_sel:WORD_0 src1_sel:WORD_1
	v_add_u32_sdwa v63, v61, v61 dst_sel:DWORD dst_unused:UNUSED_PAD src0_sel:WORD_0 src1_sel:WORD_1
	s_nop 0
	v_add_u32_dpp v62, v62, v62 quad_perm:[1,0,3,2] row_mask:0xf bank_mask:0xf bound_ctrl:1
	v_add_u32_dpp v63, v63, v63 quad_perm:[1,0,3,2] row_mask:0xf bank_mask:0xf bound_ctrl:1
	s_nop 0
	v_add_u32_dpp v62, v62, v62 quad_perm:[2,3,0,1] row_mask:0xf bank_mask:0xf bound_ctrl:1
	v_add_u32_dpp v63, v63, v63 quad_perm:[2,3,0,1] row_mask:0xf bank_mask:0xf bound_ctrl:1
	s_nop 0
	v_add_u32_dpp v62, v62, v62 row_half_mirror row_mask:0xf bank_mask:0xf bound_ctrl:1
	v_add_u32_dpp v63, v63, v63 row_half_mirror row_mask:0xf bank_mask:0xf bound_ctrl:1
	s_nop 0
	v_mov_b32_dpp v64, v62 row_mirror row_mask:0xf bank_mask:0xf bound_ctrl:1
	v_mov_b32_dpp v65, v63 row_mirror row_mask:0xf bank_mask:0xf bound_ctrl:1
	s_mov_b64 exec, s[16:17]
	v_add_u32_e32 v64, v64, v62
	v_add_u32_e32 v65, v65, v63
	ds_write_b64 v98, v[64:65] offset:2048
	s_mov_b64 exec, -1
	s_waitcnt vmcnt(15)
	v_add_u32_e32 v60, v28, v29
	v_and_b32_e32 v61, v4, v28
	v_and_b32_e32 v62, v5, v29
	v_add_u32_e32 v61, v61, v62
	v_add_u32_sdwa v62, v60, v60 dst_sel:DWORD dst_unused:UNUSED_PAD src0_sel:WORD_0 src1_sel:WORD_1
	v_add_u32_sdwa v63, v61, v61 dst_sel:DWORD dst_unused:UNUSED_PAD src0_sel:WORD_0 src1_sel:WORD_1
	s_nop 0
	v_add_u32_dpp v62, v62, v62 quad_perm:[1,0,3,2] row_mask:0xf bank_mask:0xf bound_ctrl:1
	v_add_u32_dpp v63, v63, v63 quad_perm:[1,0,3,2] row_mask:0xf bank_mask:0xf bound_ctrl:1
	s_nop 0
	v_add_u32_dpp v62, v62, v62 quad_perm:[2,3,0,1] row_mask:0xf bank_mask:0xf bound_ctrl:1
	v_add_u32_dpp v63, v63, v63 quad_perm:[2,3,0,1] row_mask:0xf bank_mask:0xf bound_ctrl:1
	s_nop 0
	v_add_u32_dpp v62, v62, v62 row_half_mirror row_mask:0xf bank_mask:0xf bound_ctrl:1
	v_add_u32_dpp v63, v63, v63 row_half_mirror row_mask:0xf bank_mask:0xf bound_ctrl:1
	s_nop 0
	v_mov_b32_dpp v64, v62 row_mirror row_mask:0xf bank_mask:0xf bound_ctrl:1
	v_mov_b32_dpp v65, v63 row_mirror row_mask:0xf bank_mask:0xf bound_ctrl:1
	s_mov_b64 exec, s[16:17]
	v_add_u32_e32 v64, v64, v62
	v_add_u32_e32 v65, v65, v63
	ds_write_b64 v98, v[64:65] offset:2304
	s_mov_b64 exec, -1
	s_waitcnt vmcnt(14)
	v_add_u32_e32 v60, v30, v31
	v_and_b32_e32 v61, v4, v30
	v_and_b32_e32 v62, v5, v31
	v_add_u32_e32 v61, v61, v62
	v_add_u32_sdwa v62, v60, v60 dst_sel:DWORD dst_unused:UNUSED_PAD src0_sel:WORD_0 src1_sel:WORD_1
	v_add_u32_sdwa v63, v61, v61 dst_sel:DWORD dst_unused:UNUSED_PAD src0_sel:WORD_0 src1_sel:WORD_1
	s_nop 0
	v_add_u32_dpp v62, v62, v62 quad_perm:[1,0,3,2] row_mask:0xf bank_mask:0xf bound_ctrl:1
	v_add_u32_dpp v63, v63, v63 quad_perm:[1,0,3,2] row_mask:0xf bank_mask:0xf bound_ctrl:1
	s_nop 0
	v_add_u32_dpp v62, v62, v62 quad_perm:[2,3,0,1] row_mask:0xf bank_mask:0xf bound_ctrl:1
	v_add_u32_dpp v63, v63, v63 quad_perm:[2,3,0,1] row_mask:0xf bank_mask:0xf bound_ctrl:1
	s_nop 0
	v_add_u32_dpp v62, v62, v62 row_half_mirror row_mask:0xf bank_mask:0xf bound_ctrl:1
	v_add_u32_dpp v63, v63, v63 row_half_mirror row_mask:0xf bank_mask:0xf bound_ctrl:1
	s_nop 0
	v_mov_b32_dpp v64, v62 row_mirror row_mask:0xf bank_mask:0xf bound_ctrl:1
	v_mov_b32_dpp v65, v63 row_mirror row_mask:0xf bank_mask:0xf bound_ctrl:1
	s_mov_b64 exec, s[16:17]
	v_add_u32_e32 v64, v64, v62
	v_add_u32_e32 v65, v65, v63
	ds_write_b64 v98, v[64:65] offset:2560
	s_mov_b64 exec, -1
	s_waitcnt vmcnt(13)
	v_add_u32_e32 v60, v32, v33
	v_and_b32_e32 v61, v4, v32
	v_and_b32_e32 v62, v5, v33
	v_add_u32_e32 v61, v61, v62
	v_add_u32_sdwa v62, v60, v60 dst_sel:DWORD dst_unused:UNUSED_PAD src0_sel:WORD_0 src1_sel:WORD_1
	v_add_u32_sdwa v63, v61, v61 dst_sel:DWORD dst_unused:UNUSED_PAD src0_sel:WORD_0 src1_sel:WORD_1
	s_nop 0
	v_add_u32_dpp v62, v62, v62 quad_perm:[1,0,3,2] row_mask:0xf bank_mask:0xf bound_ctrl:1
	v_add_u32_dpp v63, v63, v63 quad_perm:[1,0,3,2] row_mask:0xf bank_mask:0xf bound_ctrl:1
	s_nop 0
	v_add_u32_dpp v62, v62, v62 quad_perm:[2,3,0,1] row_mask:0xf bank_mask:0xf bound_ctrl:1
	v_add_u32_dpp v63, v63, v63 quad_perm:[2,3,0,1] row_mask:0xf bank_mask:0xf bound_ctrl:1
	s_nop 0
	v_add_u32_dpp v62, v62, v62 row_half_mirror row_mask:0xf bank_mask:0xf bound_ctrl:1
	v_add_u32_dpp v63, v63, v63 row_half_mirror row_mask:0xf bank_mask:0xf bound_ctrl:1
	s_nop 0
	v_mov_b32_dpp v64, v62 row_mirror row_mask:0xf bank_mask:0xf bound_ctrl:1
	v_mov_b32_dpp v65, v63 row_mirror row_mask:0xf bank_mask:0xf bound_ctrl:1
	s_mov_b64 exec, s[16:17]
	v_add_u32_e32 v64, v64, v62
	v_add_u32_e32 v65, v65, v63
	ds_write_b64 v98, v[64:65] offset:2816
	s_mov_b64 exec, -1
	s_waitcnt vmcnt(12)
	v_add_u32_e32 v60, v34, v35
	v_and_b32_e32 v61, v4, v34
	v_and_b32_e32 v62, v5, v35
	v_add_u32_e32 v61, v61, v62
	v_add_u32_sdwa v62, v60, v60 dst_sel:DWORD dst_unused:UNUSED_PAD src0_sel:WORD_0 src1_sel:WORD_1
	v_add_u32_sdwa v63, v61, v61 dst_sel:DWORD dst_unused:UNUSED_PAD src0_sel:WORD_0 src1_sel:WORD_1
	s_nop 0
	v_add_u32_dpp v62, v62, v62 quad_perm:[1,0,3,2] row_mask:0xf bank_mask:0xf bound_ctrl:1
	v_add_u32_dpp v63, v63, v63 quad_perm:[1,0,3,2] row_mask:0xf bank_mask:0xf bound_ctrl:1
	s_nop 0
	v_add_u32_dpp v62, v62, v62 quad_perm:[2,3,0,1] row_mask:0xf bank_mask:0xf bound_ctrl:1
	v_add_u32_dpp v63, v63, v63 quad_perm:[2,3,0,1] row_mask:0xf bank_mask:0xf bound_ctrl:1
	s_nop 0
	v_add_u32_dpp v62, v62, v62 row_half_mirror row_mask:0xf bank_mask:0xf bound_ctrl:1
	v_add_u32_dpp v63, v63, v63 row_half_mirror row_mask:0xf bank_mask:0xf bound_ctrl:1
	s_nop 0
	v_mov_b32_dpp v64, v62 row_mirror row_mask:0xf bank_mask:0xf bound_ctrl:1
	v_mov_b32_dpp v65, v63 row_mirror row_mask:0xf bank_mask:0xf bound_ctrl:1
	s_mov_b64 exec, s[16:17]
	v_add_u32_e32 v64, v64, v62
	v_add_u32_e32 v65, v65, v63
	ds_write_b64 v98, v[64:65] offset:3072
	s_mov_b64 exec, -1
	s_waitcnt vmcnt(11)
	v_add_u32_e32 v60, v36, v37
	v_and_b32_e32 v61, v4, v36
	v_and_b32_e32 v62, v5, v37
	v_add_u32_e32 v61, v61, v62
	v_add_u32_sdwa v62, v60, v60 dst_sel:DWORD dst_unused:UNUSED_PAD src0_sel:WORD_0 src1_sel:WORD_1
	v_add_u32_sdwa v63, v61, v61 dst_sel:DWORD dst_unused:UNUSED_PAD src0_sel:WORD_0 src1_sel:WORD_1
	s_nop 0
	v_add_u32_dpp v62, v62, v62 quad_perm:[1,0,3,2] row_mask:0xf bank_mask:0xf bound_ctrl:1
	v_add_u32_dpp v63, v63, v63 quad_perm:[1,0,3,2] row_mask:0xf bank_mask:0xf bound_ctrl:1
	s_nop 0
	v_add_u32_dpp v62, v62, v62 quad_perm:[2,3,0,1] row_mask:0xf bank_mask:0xf bound_ctrl:1
	v_add_u32_dpp v63, v63, v63 quad_perm:[2,3,0,1] row_mask:0xf bank_mask:0xf bound_ctrl:1
	s_nop 0
	v_add_u32_dpp v62, v62, v62 row_half_mirror row_mask:0xf bank_mask:0xf bound_ctrl:1
	v_add_u32_dpp v63, v63, v63 row_half_mirror row_mask:0xf bank_mask:0xf bound_ctrl:1
	s_nop 0
	v_mov_b32_dpp v64, v62 row_mirror row_mask:0xf bank_mask:0xf bound_ctrl:1
	v_mov_b32_dpp v65, v63 row_mirror row_mask:0xf bank_mask:0xf bound_ctrl:1
	s_mov_b64 exec, s[16:17]
	v_add_u32_e32 v64, v64, v62
	v_add_u32_e32 v65, v65, v63
	ds_write_b64 v98, v[64:65] offset:3328
	s_mov_b64 exec, -1
	s_waitcnt vmcnt(10)
	v_add_u32_e32 v60, v38, v39
	v_and_b32_e32 v61, v4, v38
	v_and_b32_e32 v62, v5, v39
	v_add_u32_e32 v61, v61, v62
	v_add_u32_sdwa v62, v60, v60 dst_sel:DWORD dst_unused:UNUSED_PAD src0_sel:WORD_0 src1_sel:WORD_1
	v_add_u32_sdwa v63, v61, v61 dst_sel:DWORD dst_unused:UNUSED_PAD src0_sel:WORD_0 src1_sel:WORD_1
	s_nop 0
	v_add_u32_dpp v62, v62, v62 quad_perm:[1,0,3,2] row_mask:0xf bank_mask:0xf bound_ctrl:1
	v_add_u32_dpp v63, v63, v63 quad_perm:[1,0,3,2] row_mask:0xf bank_mask:0xf bound_ctrl:1
	s_nop 0
	v_add_u32_dpp v62, v62, v62 quad_perm:[2,3,0,1] row_mask:0xf bank_mask:0xf bound_ctrl:1
	v_add_u32_dpp v63, v63, v63 quad_perm:[2,3,0,1] row_mask:0xf bank_mask:0xf bound_ctrl:1
	s_nop 0
	v_add_u32_dpp v62, v62, v62 row_half_mirror row_mask:0xf bank_mask:0xf bound_ctrl:1
	v_add_u32_dpp v63, v63, v63 row_half_mirror row_mask:0xf bank_mask:0xf bound_ctrl:1
	s_nop 0
	v_mov_b32_dpp v64, v62 row_mirror row_mask:0xf bank_mask:0xf bound_ctrl:1
	v_mov_b32_dpp v65, v63 row_mirror row_mask:0xf bank_mask:0xf bound_ctrl:1
	s_mov_b64 exec, s[16:17]
	v_add_u32_e32 v64, v64, v62
	v_add_u32_e32 v65, v65, v63
	ds_write_b64 v98, v[64:65] offset:3584
	s_mov_b64 exec, -1
	s_waitcnt vmcnt(9)
	v_add_u32_e32 v60, v40, v41
	v_and_b32_e32 v61, v4, v40
	v_and_b32_e32 v62, v5, v41
	v_add_u32_e32 v61, v61, v62
	v_add_u32_sdwa v62, v60, v60 dst_sel:DWORD dst_unused:UNUSED_PAD src0_sel:WORD_0 src1_sel:WORD_1
	v_add_u32_sdwa v63, v61, v61 dst_sel:DWORD dst_unused:UNUSED_PAD src0_sel:WORD_0 src1_sel:WORD_1
	s_nop 0
	v_add_u32_dpp v62, v62, v62 quad_perm:[1,0,3,2] row_mask:0xf bank_mask:0xf bound_ctrl:1
	v_add_u32_dpp v63, v63, v63 quad_perm:[1,0,3,2] row_mask:0xf bank_mask:0xf bound_ctrl:1
	s_nop 0
	v_add_u32_dpp v62, v62, v62 quad_perm:[2,3,0,1] row_mask:0xf bank_mask:0xf bound_ctrl:1
	v_add_u32_dpp v63, v63, v63 quad_perm:[2,3,0,1] row_mask:0xf bank_mask:0xf bound_ctrl:1
	s_nop 0
	v_add_u32_dpp v62, v62, v62 row_half_mirror row_mask:0xf bank_mask:0xf bound_ctrl:1
	v_add_u32_dpp v63, v63, v63 row_half_mirror row_mask:0xf bank_mask:0xf bound_ctrl:1
	s_nop 0
	v_mov_b32_dpp v64, v62 row_mirror row_mask:0xf bank_mask:0xf bound_ctrl:1
	v_mov_b32_dpp v65, v63 row_mirror row_mask:0xf bank_mask:0xf bound_ctrl:1
	s_mov_b64 exec, s[16:17]
	v_add_u32_e32 v64, v64, v62
	v_add_u32_e32 v65, v65, v63
	ds_write_b64 v98, v[64:65] offset:3840
	s_mov_b64 exec, -1
	s_waitcnt vmcnt(8)
	v_add_u32_e32 v60, v42, v43
	v_and_b32_e32 v61, v4, v42
	v_and_b32_e32 v62, v5, v43
	v_add_u32_e32 v61, v61, v62
	v_add_u32_sdwa v62, v60, v60 dst_sel:DWORD dst_unused:UNUSED_PAD src0_sel:WORD_0 src1_sel:WORD_1
	v_add_u32_sdwa v63, v61, v61 dst_sel:DWORD dst_unused:UNUSED_PAD src0_sel:WORD_0 src1_sel:WORD_1
	s_nop 0
	v_add_u32_dpp v62, v62, v62 quad_perm:[1,0,3,2] row_mask:0xf bank_mask:0xf bound_ctrl:1
	v_add_u32_dpp v63, v63, v63 quad_perm:[1,0,3,2] row_mask:0xf bank_mask:0xf bound_ctrl:1
	s_nop 0
	v_add_u32_dpp v62, v62, v62 quad_perm:[2,3,0,1] row_mask:0xf bank_mask:0xf bound_ctrl:1
	v_add_u32_dpp v63, v63, v63 quad_perm:[2,3,0,1] row_mask:0xf bank_mask:0xf bound_ctrl:1
	s_nop 0
	v_add_u32_dpp v62, v62, v62 row_half_mirror row_mask:0xf bank_mask:0xf bound_ctrl:1
	v_add_u32_dpp v63, v63, v63 row_half_mirror row_mask:0xf bank_mask:0xf bound_ctrl:1
	s_nop 0
	v_mov_b32_dpp v64, v62 row_mirror row_mask:0xf bank_mask:0xf bound_ctrl:1
	v_mov_b32_dpp v65, v63 row_mirror row_mask:0xf bank_mask:0xf bound_ctrl:1
	s_mov_b64 exec, s[16:17]
	v_add_u32_e32 v64, v64, v62
	v_add_u32_e32 v65, v65, v63
	ds_write_b64 v98, v[64:65] offset:4096
	s_mov_b64 exec, -1
	s_waitcnt vmcnt(7)
	v_add_u32_e32 v60, v44, v45
	v_and_b32_e32 v61, v4, v44
	v_and_b32_e32 v62, v5, v45
	v_add_u32_e32 v61, v61, v62
	v_add_u32_sdwa v62, v60, v60 dst_sel:DWORD dst_unused:UNUSED_PAD src0_sel:WORD_0 src1_sel:WORD_1
	v_add_u32_sdwa v63, v61, v61 dst_sel:DWORD dst_unused:UNUSED_PAD src0_sel:WORD_0 src1_sel:WORD_1
	s_nop 0
	v_add_u32_dpp v62, v62, v62 quad_perm:[1,0,3,2] row_mask:0xf bank_mask:0xf bound_ctrl:1
	v_add_u32_dpp v63, v63, v63 quad_perm:[1,0,3,2] row_mask:0xf bank_mask:0xf bound_ctrl:1
	s_nop 0
	v_add_u32_dpp v62, v62, v62 quad_perm:[2,3,0,1] row_mask:0xf bank_mask:0xf bound_ctrl:1
	v_add_u32_dpp v63, v63, v63 quad_perm:[2,3,0,1] row_mask:0xf bank_mask:0xf bound_ctrl:1
	s_nop 0
	v_add_u32_dpp v62, v62, v62 row_half_mirror row_mask:0xf bank_mask:0xf bound_ctrl:1
	v_add_u32_dpp v63, v63, v63 row_half_mirror row_mask:0xf bank_mask:0xf bound_ctrl:1
	s_nop 0
	v_mov_b32_dpp v64, v62 row_mirror row_mask:0xf bank_mask:0xf bound_ctrl:1
	v_mov_b32_dpp v65, v63 row_mirror row_mask:0xf bank_mask:0xf bound_ctrl:1
	s_mov_b64 exec, s[16:17]
	v_add_u32_e32 v64, v64, v62
	v_add_u32_e32 v65, v65, v63
	ds_write_b64 v98, v[64:65] offset:4352
	s_mov_b64 exec, -1
	s_waitcnt vmcnt(6)
	v_add_u32_e32 v60, v46, v47
	v_and_b32_e32 v61, v4, v46
	v_and_b32_e32 v62, v5, v47
	v_add_u32_e32 v61, v61, v62
	v_add_u32_sdwa v62, v60, v60 dst_sel:DWORD dst_unused:UNUSED_PAD src0_sel:WORD_0 src1_sel:WORD_1
	v_add_u32_sdwa v63, v61, v61 dst_sel:DWORD dst_unused:UNUSED_PAD src0_sel:WORD_0 src1_sel:WORD_1
	s_nop 0
	v_add_u32_dpp v62, v62, v62 quad_perm:[1,0,3,2] row_mask:0xf bank_mask:0xf bound_ctrl:1
	v_add_u32_dpp v63, v63, v63 quad_perm:[1,0,3,2] row_mask:0xf bank_mask:0xf bound_ctrl:1
	s_nop 0
	v_add_u32_dpp v62, v62, v62 quad_perm:[2,3,0,1] row_mask:0xf bank_mask:0xf bound_ctrl:1
	v_add_u32_dpp v63, v63, v63 quad_perm:[2,3,0,1] row_mask:0xf bank_mask:0xf bound_ctrl:1
	s_nop 0
	v_add_u32_dpp v62, v62, v62 row_half_mirror row_mask:0xf bank_mask:0xf bound_ctrl:1
	v_add_u32_dpp v63, v63, v63 row_half_mirror row_mask:0xf bank_mask:0xf bound_ctrl:1
	s_nop 0
	v_mov_b32_dpp v64, v62 row_mirror row_mask:0xf bank_mask:0xf bound_ctrl:1
	v_mov_b32_dpp v65, v63 row_mirror row_mask:0xf bank_mask:0xf bound_ctrl:1
	s_mov_b64 exec, s[16:17]
	v_add_u32_e32 v64, v64, v62
	v_add_u32_e32 v65, v65, v63
	ds_write_b64 v98, v[64:65] offset:4608
	s_mov_b64 exec, -1
	s_waitcnt vmcnt(5)
	v_add_u32_e32 v60, v48, v49
	v_and_b32_e32 v61, v4, v48
	v_and_b32_e32 v62, v5, v49
	v_add_u32_e32 v61, v61, v62
	v_add_u32_sdwa v62, v60, v60 dst_sel:DWORD dst_unused:UNUSED_PAD src0_sel:WORD_0 src1_sel:WORD_1
	v_add_u32_sdwa v63, v61, v61 dst_sel:DWORD dst_unused:UNUSED_PAD src0_sel:WORD_0 src1_sel:WORD_1
	s_nop 0
	v_add_u32_dpp v62, v62, v62 quad_perm:[1,0,3,2] row_mask:0xf bank_mask:0xf bound_ctrl:1
	v_add_u32_dpp v63, v63, v63 quad_perm:[1,0,3,2] row_mask:0xf bank_mask:0xf bound_ctrl:1
	s_nop 0
	v_add_u32_dpp v62, v62, v62 quad_perm:[2,3,0,1] row_mask:0xf bank_mask:0xf bound_ctrl:1
	v_add_u32_dpp v63, v63, v63 quad_perm:[2,3,0,1] row_mask:0xf bank_mask:0xf bound_ctrl:1
	s_nop 0
	v_add_u32_dpp v62, v62, v62 row_half_mirror row_mask:0xf bank_mask:0xf bound_ctrl:1
	v_add_u32_dpp v63, v63, v63 row_half_mirror row_mask:0xf bank_mask:0xf bound_ctrl:1
	s_nop 0
	v_mov_b32_dpp v64, v62 row_mirror row_mask:0xf bank_mask:0xf bound_ctrl:1
	v_mov_b32_dpp v65, v63 row_mirror row_mask:0xf bank_mask:0xf bound_ctrl:1
	s_mov_b64 exec, s[16:17]
	v_add_u32_e32 v64, v64, v62
	v_add_u32_e32 v65, v65, v63
	ds_write_b64 v98, v[64:65] offset:4864
	s_mov_b64 exec, -1
	s_waitcnt vmcnt(4)
	v_add_u32_e32 v60, v50, v51
	v_and_b32_e32 v61, v4, v50
	v_and_b32_e32 v62, v5, v51
	v_add_u32_e32 v61, v61, v62
	v_add_u32_sdwa v62, v60, v60 dst_sel:DWORD dst_unused:UNUSED_PAD src0_sel:WORD_0 src1_sel:WORD_1
	v_add_u32_sdwa v63, v61, v61 dst_sel:DWORD dst_unused:UNUSED_PAD src0_sel:WORD_0 src1_sel:WORD_1
	s_nop 0
	v_add_u32_dpp v62, v62, v62 quad_perm:[1,0,3,2] row_mask:0xf bank_mask:0xf bound_ctrl:1
	v_add_u32_dpp v63, v63, v63 quad_perm:[1,0,3,2] row_mask:0xf bank_mask:0xf bound_ctrl:1
	s_nop 0
	v_add_u32_dpp v62, v62, v62 quad_perm:[2,3,0,1] row_mask:0xf bank_mask:0xf bound_ctrl:1
	v_add_u32_dpp v63, v63, v63 quad_perm:[2,3,0,1] row_mask:0xf bank_mask:0xf bound_ctrl:1
	s_nop 0
	v_add_u32_dpp v62, v62, v62 row_half_mirror row_mask:0xf bank_mask:0xf bound_ctrl:1
	v_add_u32_dpp v63, v63, v63 row_half_mirror row_mask:0xf bank_mask:0xf bound_ctrl:1
	s_nop 0
	v_mov_b32_dpp v64, v62 row_mirror row_mask:0xf bank_mask:0xf bound_ctrl:1
	v_mov_b32_dpp v65, v63 row_mirror row_mask:0xf bank_mask:0xf bound_ctrl:1
	s_mov_b64 exec, s[16:17]
	v_add_u32_e32 v64, v64, v62
	v_add_u32_e32 v65, v65, v63
	ds_write_b64 v98, v[64:65] offset:5120
	s_mov_b64 exec, -1
	s_waitcnt vmcnt(3)
	v_add_u32_e32 v60, v52, v53
	v_and_b32_e32 v61, v4, v52
	v_and_b32_e32 v62, v5, v53
	v_add_u32_e32 v61, v61, v62
	v_add_u32_sdwa v62, v60, v60 dst_sel:DWORD dst_unused:UNUSED_PAD src0_sel:WORD_0 src1_sel:WORD_1
	v_add_u32_sdwa v63, v61, v61 dst_sel:DWORD dst_unused:UNUSED_PAD src0_sel:WORD_0 src1_sel:WORD_1
	s_nop 0
	v_add_u32_dpp v62, v62, v62 quad_perm:[1,0,3,2] row_mask:0xf bank_mask:0xf bound_ctrl:1
	v_add_u32_dpp v63, v63, v63 quad_perm:[1,0,3,2] row_mask:0xf bank_mask:0xf bound_ctrl:1
	s_nop 0
	v_add_u32_dpp v62, v62, v62 quad_perm:[2,3,0,1] row_mask:0xf bank_mask:0xf bound_ctrl:1
	v_add_u32_dpp v63, v63, v63 quad_perm:[2,3,0,1] row_mask:0xf bank_mask:0xf bound_ctrl:1
	s_nop 0
	v_add_u32_dpp v62, v62, v62 row_half_mirror row_mask:0xf bank_mask:0xf bound_ctrl:1
	v_add_u32_dpp v63, v63, v63 row_half_mirror row_mask:0xf bank_mask:0xf bound_ctrl:1
	s_nop 0
	v_mov_b32_dpp v64, v62 row_mirror row_mask:0xf bank_mask:0xf bound_ctrl:1
	v_mov_b32_dpp v65, v63 row_mirror row_mask:0xf bank_mask:0xf bound_ctrl:1
	s_mov_b64 exec, s[16:17]
	v_add_u32_e32 v64, v64, v62
	v_add_u32_e32 v65, v65, v63
	ds_write_b64 v98, v[64:65] offset:5376
	s_mov_b64 exec, -1
	s_waitcnt vmcnt(2)
	v_add_u32_e32 v60, v54, v55
	v_and_b32_e32 v61, v4, v54
	v_and_b32_e32 v62, v5, v55
	v_add_u32_e32 v61, v61, v62
	v_add_u32_sdwa v62, v60, v60 dst_sel:DWORD dst_unused:UNUSED_PAD src0_sel:WORD_0 src1_sel:WORD_1
	v_add_u32_sdwa v63, v61, v61 dst_sel:DWORD dst_unused:UNUSED_PAD src0_sel:WORD_0 src1_sel:WORD_1
	s_nop 0
	v_add_u32_dpp v62, v62, v62 quad_perm:[1,0,3,2] row_mask:0xf bank_mask:0xf bound_ctrl:1
	v_add_u32_dpp v63, v63, v63 quad_perm:[1,0,3,2] row_mask:0xf bank_mask:0xf bound_ctrl:1
	s_nop 0
	v_add_u32_dpp v62, v62, v62 quad_perm:[2,3,0,1] row_mask:0xf bank_mask:0xf bound_ctrl:1
	v_add_u32_dpp v63, v63, v63 quad_perm:[2,3,0,1] row_mask:0xf bank_mask:0xf bound_ctrl:1
	s_nop 0
	v_add_u32_dpp v62, v62, v62 row_half_mirror row_mask:0xf bank_mask:0xf bound_ctrl:1
	v_add_u32_dpp v63, v63, v63 row_half_mirror row_mask:0xf bank_mask:0xf bound_ctrl:1
	s_nop 0
	v_mov_b32_dpp v64, v62 row_mirror row_mask:0xf bank_mask:0xf bound_ctrl:1
	v_mov_b32_dpp v65, v63 row_mirror row_mask:0xf bank_mask:0xf bound_ctrl:1
	s_mov_b64 exec, s[16:17]
	v_add_u32_e32 v64, v64, v62
	v_add_u32_e32 v65, v65, v63
	ds_write_b64 v98, v[64:65] offset:5632
	s_mov_b64 exec, -1
	s_waitcnt vmcnt(1)
	v_add_u32_e32 v60, v56, v57
	v_and_b32_e32 v61, v4, v56
	v_and_b32_e32 v62, v5, v57
	v_add_u32_e32 v61, v61, v62
	v_add_u32_sdwa v62, v60, v60 dst_sel:DWORD dst_unused:UNUSED_PAD src0_sel:WORD_0 src1_sel:WORD_1
	v_add_u32_sdwa v63, v61, v61 dst_sel:DWORD dst_unused:UNUSED_PAD src0_sel:WORD_0 src1_sel:WORD_1
	s_nop 0
	v_add_u32_dpp v62, v62, v62 quad_perm:[1,0,3,2] row_mask:0xf bank_mask:0xf bound_ctrl:1
	v_add_u32_dpp v63, v63, v63 quad_perm:[1,0,3,2] row_mask:0xf bank_mask:0xf bound_ctrl:1
	s_nop 0
	v_add_u32_dpp v62, v62, v62 quad_perm:[2,3,0,1] row_mask:0xf bank_mask:0xf bound_ctrl:1
	v_add_u32_dpp v63, v63, v63 quad_perm:[2,3,0,1] row_mask:0xf bank_mask:0xf bound_ctrl:1
	s_nop 0
	v_add_u32_dpp v62, v62, v62 row_half_mirror row_mask:0xf bank_mask:0xf bound_ctrl:1
	v_add_u32_dpp v63, v63, v63 row_half_mirror row_mask:0xf bank_mask:0xf bound_ctrl:1
	s_nop 0
	v_mov_b32_dpp v64, v62 row_mirror row_mask:0xf bank_mask:0xf bound_ctrl:1
	v_mov_b32_dpp v65, v63 row_mirror row_mask:0xf bank_mask:0xf bound_ctrl:1
	s_mov_b64 exec, s[16:17]
	v_add_u32_e32 v64, v64, v62
	v_add_u32_e32 v65, v65, v63
	ds_write_b64 v98, v[64:65] offset:5888
	s_mov_b64 exec, -1
	s_waitcnt vmcnt(0)
	v_add_u32_e32 v60, v58, v59
	v_and_b32_e32 v61, v4, v58
	v_and_b32_e32 v62, v5, v59
	v_add_u32_e32 v61, v61, v62
	v_add_u32_sdwa v62, v60, v60 dst_sel:DWORD dst_unused:UNUSED_PAD src0_sel:WORD_0 src1_sel:WORD_1
	v_add_u32_sdwa v63, v61, v61 dst_sel:DWORD dst_unused:UNUSED_PAD src0_sel:WORD_0 src1_sel:WORD_1
	s_nop 0
	v_add_u32_dpp v62, v62, v62 quad_perm:[1,0,3,2] row_mask:0xf bank_mask:0xf bound_ctrl:1
	v_add_u32_dpp v63, v63, v63 quad_perm:[1,0,3,2] row_mask:0xf bank_mask:0xf bound_ctrl:1
	s_nop 0
	v_add_u32_dpp v62, v62, v62 quad_perm:[2,3,0,1] row_mask:0xf bank_mask:0xf bound_ctrl:1
	v_add_u32_dpp v63, v63, v63 quad_perm:[2,3,0,1] row_mask:0xf bank_mask:0xf bound_ctrl:1
	s_nop 0
	v_add_u32_dpp v62, v62, v62 row_half_mirror row_mask:0xf bank_mask:0xf bound_ctrl:1
	v_add_u32_dpp v63, v63, v63 row_half_mirror row_mask:0xf bank_mask:0xf bound_ctrl:1
	s_nop 0
	v_mov_b32_dpp v64, v62 row_mirror row_mask:0xf bank_mask:0xf bound_ctrl:1
	v_mov_b32_dpp v65, v63 row_mirror row_mask:0xf bank_mask:0xf bound_ctrl:1
	s_mov_b64 exec, s[18:19]
	v_add_u32_e32 v64, v64, v62
	v_add_u32_e32 v65, v65, v63
	ds_write_b64 v98, v[64:65] offset:6144
	s_mov_b64 exec, -1
	s_movk_i32 s3, 0x100
	v_cmp_gt_u32_e32 vcc, s3, v0
	v_lshlrev_b32_e32 v2, 2, v0
	s_and_saveexec_b64 s[4:5], vcc
	v_mov_b32_e32 v3, 0
	ds_write_b32 v2, v3 offset:7296
	s_or_b64 exec, exec, s[4:5]
	s_load_dwordx4 s[4:7], s[34:35], 0x10
	s_waitcnt lgkmcnt(0)
	s_barrier
	s_and_saveexec_b64 s[0:1], vcc
	s_cbranch_execz .LBB1_73
	s_movk_i32 s3, 0xc4
	v_cmp_gt_u32_e32 vcc, s3, v0
	v_mov_b32_e32 v3, 0
	v_mov_b32_e32 v4, 0
	s_and_saveexec_b64 s[8:9], vcc
	s_cbranch_execz .LBB1_72
	v_lshlrev_b32_e32 v3, 5, v0
	ds_read2_b64 v[4:7], v3 offset1:1
	ds_read2_b64 v[8:11], v3 offset0:2 offset1:3
	s_waitcnt lgkmcnt(1)
	v_add_u32_e32 v5, v5, v7
	v_add_u32_e32 v3, v6, v4
	s_waitcnt lgkmcnt(0)
	v_add3_u32 v3, v8, v3, v10
	v_add3_u32 v4, v9, v5, v11
